# SB step in the positive-log domain: 29 of 32 v_xor negations removed (logs write the target register), consumers use v_sub, finish test flipped
# speedup vs baseline: 1.0122x; 1.0007x over previous
; #define LAS __attribute__((address_space(3)))
; __device__ __forceinline__ float ex2(float x) { return __builtin_amdgcn_exp2f(x); }
; __device__ __forceinline__ float lg2(float x) { return __builtin_amdgcn_logf(x); }
; __device__ __forceinline__ f32x16 mfma32(bf16x8 a, bf16x8 b, f32x16 c) { return __builtin_amdgcn_mfma_f32_32x32x16_bf16(a, b, c, 0, 0, 0); }
; #define SB_DMA(t, s) do { glds(ksrc + (size_t)(t) * 64 * INP, shm + (s) * KS_SB + wid * 1024); glds(vsrc + (size_t)(t) * 64 * INP, shm + SB_VOFF + (s) * VS + wid * 1024); } while (0)
; #define SB_WAITBAR() asm volatile("s_waitcnt vmcnt(4) lgkmcnt(0)\n\ts_barrier" ::: "memory")
; __device__ __forceinline__ void sb_unit(int b, int h, int qb, const bf16_t* __restrict__ PROJ, bf16_t* OCAT, float* SSQO, ldsp shm, volatile LAS unsigned* FL) {
;     ...
;         SB_WAITBAR();
;         if (step > 0) { if (FL[(step - 1) % 3] == 0xFFu) break; }
;         if (tid == 0) FL[(step + 1) % 3] = 0u;
;         SB_DMA(SB_TILE(step + 3), (step + 3) & 3);
;         if (t <= tdw && !wfin) {
;             const LAS unsigned char* kb = shm + (step & 3) * KS_SB + hi * 1024 + r32 * 16;
;             f32x16 z0 = f32x16{}, z1 = f32x16{};
; #pragma unroll
;             for (int d0 = 0; d0 < 4; ++d0) { const bf16x8 k0 = *(const LAS bf16x8*)(kb + d0 * 2048), k1 = *(const LAS bf16x8*)(kb + d0 * 2048 + 512);
;                 z0 = mfma32(k0, qr[d0], z0); z1 = mfma32(k1, qr[d0], z1); }
;             const bool diag = (t == tdw); const int kb0 = t * 64 + 4 * hi;
;             f32x16 l0, l1; float tot = 0.f;
; #pragma unroll
;             for (int r = 0; r < 16; ++r) { l0[r] = -lg2(1.0f + ex2(fminf(z0[r], 100.f))); l1[r] = -lg2(1.0f + ex2(fminf(z1[r], 100.f))); }
.LBB0_1055:
	s_or_b64 exec, exec, s[4:5]
	s_add_i32 s6, s34, s2
	s_max_i32 s8, s6, 0
	s_add_i32 s7, s3, 0x6000
	s_lshl_b64 s[4:5], s[8:9], 18
	s_and_b32 s7, s7, 0x6000
	v_lshl_add_u64 v[38:39], v[154:155], 0, s[4:5]
	s_add_i32 s7, s26, s7
	v_lshl_add_u64 v[38:39], v[38:39], 0, s[82:83]
	s_mov_b32 m0, s7
	s_add_i32 s6, s6, 3
	global_load_lds_dwordx4 v[38:39], off
	v_lshl_add_u64 v[38:39], v[156:157], 0, s[4:5]
	v_lshl_add_u64 v[38:39], v[38:39], 0, s[84:85]
	s_add_i32 m0, s7, 0x8000
	s_cmp_gt_i32 s6, s35
	global_load_lds_dwordx4 v[38:39], off
	s_cselect_b64 s[4:5], -1, 0
	s_or_b64 s[4:5], s[0:1], s[4:5]
	s_and_b64 vcc, exec, s[4:5]
	s_cbranch_vccnz .LBB0_1061
	s_and_b32 s8, s3, 0x6000
	v_add_u32_e32 v1, s8, v164
	ds_read_b128 v[38:41], v1
	ds_read_b128 v[42:45], v1 offset:512
	s_cmp_eq_u32 s27, s2
	s_cselect_b64 s[16:17], -1, 0
	s_cmp_lg_u32 s27, s2
	s_waitcnt lgkmcnt(0)
	v_mfma_f32_32x32x16_bf16 v[98:113], v[38:41], v[130:133], 0
	v_mfma_f32_32x32x16_bf16 v[82:97], v[42:45], v[130:133], 0
	ds_read_b128 v[38:41], v1 offset:2048
	ds_read_b128 v[42:45], v1 offset:2560
	s_waitcnt lgkmcnt(0)
	v_mfma_f32_32x32x16_bf16 v[82:97], v[42:45], v[134:137], v[82:97]
	v_mfma_f32_32x32x16_bf16 v[98:113], v[38:41], v[134:137], v[98:113]
	ds_read_b128 v[38:41], v1 offset:4096
	ds_read_b128 v[42:45], v1 offset:4608
	s_waitcnt lgkmcnt(0)
	v_mfma_f32_32x32x16_bf16 v[82:97], v[42:45], v[138:141], v[82:97]
	v_mfma_f32_32x32x16_bf16 v[98:113], v[38:41], v[138:141], v[98:113]
	ds_read_b128 v[38:41], v1 offset:6144
	ds_read_b128 v[42:45], v1 offset:6656
	s_waitcnt lgkmcnt(0)
	v_mfma_f32_32x32x16_bf16 v[82:97], v[42:45], v[142:145], v[82:97]
	v_mfma_f32_32x32x16_bf16 v[98:113], v[38:41], v[142:145], v[98:113]
	s_nop 10
	v_min_f32_e32 v2, 0x42c80000, v82
	v_exp_f32_e32 v2, v2
	v_min_f32_e32 v60, 0x42c80000, v94
	v_exp_f32_e32 v60, v60
	v_add_f32_e32 v2, 1.0, v2
	v_min_f32_e32 v37, 0x42c80000, v99
	v_exp_f32_e32 v37, v37
	v_min_f32_e32 v1, 0x42c80000, v98
	v_exp_f32_e32 v1, v1
	v_log_f32_e32 v52, v2
	v_add_f32_e32 v2, 1.0, v37
	v_log_f32_e32 v37, v2
	v_add_f32_e32 v1, 1.0, v1
	v_min_f32_e32 v2, 0x42c80000, v83
	v_log_f32_e32 v1, v1
	v_exp_f32_e32 v39, v2
	v_mov_b32_e32 v2, v1
	v_mov_b32_e32 v1, v37
	v_add_f32_e32 v37, 1.0, v39
	v_min_f32_e32 v38, 0x42c80000, v100
	v_min_f32_e32 v39, 0x42c80000, v84
	v_exp_f32_e32 v38, v38
	v_exp_f32_e32 v39, v39
	v_min_f32_e32 v59, 0x42c80000, v110
	v_exp_f32_e32 v59, v59
	v_add_f32_e32 v38, 1.0, v38
	v_add_f32_e32 v39, 1.0, v39
	v_log_f32_e32 v54, v38
	v_log_f32_e32 v56, v39
	v_add_f32_e32 v59, 1.0, v59
	v_log_f32_e32 v74, v59
	v_add_f32_e32 v59, 1.0, v60
	v_min_f32_e32 v60, 0x42c80000, v111
	v_min_f32_e32 v40, 0x42c80000, v101
	v_exp_f32_e32 v60, v60
	v_min_f32_e32 v61, 0x42c80000, v95
	v_log_f32_e32 v53, v37
	v_exp_f32_e32 v40, v40
	v_min_f32_e32 v38, 0x42c80000, v85
	v_min_f32_e32 v39, 0x42c80000, v102
	v_exp_f32_e32 v61, v61
	v_exp_f32_e32 v38, v38
	v_exp_f32_e32 v39, v39
	v_log_f32_e32 v76, v59
	v_add_f32_e32 v59, 1.0, v60
	v_add_f32_e32 v37, 1.0, v40
	v_log_f32_e32 v75, v59
	v_add_f32_e32 v59, 1.0, v61
	v_min_f32_e32 v60, 0x42c80000, v112
	v_add_f32_e32 v38, 1.0, v38
	v_add_f32_e32 v39, 1.0, v39
	v_min_f32_e32 v40, 0x42c80000, v86
	v_exp_f32_e32 v60, v60
	v_min_f32_e32 v61, 0x42c80000, v96
	v_log_f32_e32 v55, v37
	v_log_f32_e32 v57, v38
	v_log_f32_e32 v58, v39
	v_exp_f32_e32 v40, v40
	v_exp_f32_e32 v61, v61
	v_log_f32_e32 v77, v59
	v_add_f32_e32 v59, 1.0, v60
	v_add_f32_e32 v37, 1.0, v40
	v_log_f32_e32 v78, v59
	v_add_f32_e32 v59, 1.0, v61
	v_min_f32_e32 v60, 0x42c80000, v113
	v_min_f32_e32 v38, 0x42c80000, v103
	v_min_f32_e32 v39, 0x42c80000, v87
	v_min_f32_e32 v40, 0x42c80000, v104
	v_min_f32_e32 v41, 0x42c80000, v88
	v_min_f32_e32 v42, 0x42c80000, v105
	v_min_f32_e32 v43, 0x42c80000, v89
	v_min_f32_e32 v44, 0x42c80000, v106
	v_min_f32_e32 v45, 0x42c80000, v90
	v_min_f32_e32 v46, 0x42c80000, v107
	v_min_f32_e32 v47, 0x42c80000, v91
	v_min_f32_e32 v48, 0x42c80000, v108
	v_min_f32_e32 v49, 0x42c80000, v92
	v_min_f32_e32 v50, 0x42c80000, v109
	v_min_f32_e32 v51, 0x42c80000, v93
	v_exp_f32_e32 v60, v60
	v_min_f32_e32 v61, 0x42c80000, v97
	v_exp_f32_e32 v38, v38
	v_exp_f32_e32 v39, v39
	v_exp_f32_e32 v40, v40
	v_exp_f32_e32 v41, v41
	v_exp_f32_e32 v42, v42
	v_exp_f32_e32 v43, v43
	v_exp_f32_e32 v44, v44
	v_exp_f32_e32 v45, v45
	v_exp_f32_e32 v46, v46
	v_exp_f32_e32 v47, v47
	v_exp_f32_e32 v48, v48
	v_exp_f32_e32 v49, v49
	v_exp_f32_e32 v50, v50
	v_exp_f32_e32 v51, v51
	v_exp_f32_e32 v61, v61
	v_log_f32_e32 v80, v59
	v_add_f32_e32 v59, 1.0, v60
	v_add_f32_e32 v38, 1.0, v38
	v_add_f32_e32 v39, 1.0, v39
	v_add_f32_e32 v40, 1.0, v40
	v_add_f32_e32 v41, 1.0, v41
	v_add_f32_e32 v42, 1.0, v42
	v_add_f32_e32 v43, 1.0, v43
	v_add_f32_e32 v44, 1.0, v44
	v_add_f32_e32 v45, 1.0, v45
	v_add_f32_e32 v46, 1.0, v46
	v_add_f32_e32 v47, 1.0, v47
	v_add_f32_e32 v48, 1.0, v48
	v_add_f32_e32 v49, 1.0, v49
	v_add_f32_e32 v50, 1.0, v50
	v_add_f32_e32 v51, 1.0, v51
	v_log_f32_e32 v79, v59
	v_add_f32_e32 v59, 1.0, v61
	v_log_f32_e32 v60, v37
	v_log_f32_e32 v38, v38
	v_log_f32_e32 v61, v39
	v_log_f32_e32 v62, v40
	v_log_f32_e32 v64, v41
	v_log_f32_e32 v63, v42
	v_log_f32_e32 v65, v43
	v_log_f32_e32 v66, v44
	v_log_f32_e32 v68, v45
	v_log_f32_e32 v67, v46
	v_log_f32_e32 v69, v47
	v_log_f32_e32 v70, v48
	v_log_f32_e32 v72, v49
	v_log_f32_e32 v71, v50
	v_log_f32_e32 v73, v51
	v_log_f32_e32 v81, v59
	v_mov_b32_e32 v59, v38
	s_cbranch_scc1 .LBB0_1058
; __device__ __forceinline__ void sb_unit(int b, int h, int qb, const bf16_t* __restrict__ PROJ, bf16_t* OCAT, float* SSQO, ldsp shm, volatile LAS unsigned* FL) {
;     ...
;             if (diag) {
; #pragma unroll
;                 for (int r = 0; r < 16; ++r) { const int kk = kb0 + (r & 3) + 8 * (r >> 2); if (kk >= qabs) l0[r] = 0.f; if (kk + 32 >= qabs) l1[r] = 0.f; } }
	v_add_u32_e32 v166, s33, v165
	v_add_u32_e32 v167, 0xc0, v166
	v_add_u32_e32 v168, 0xe0, v166
	v_add_u32_e32 v169, 0xc1, v166
	v_add_u32_e32 v170, 0xe1, v166
	v_add_u32_e32 v171, 0xc2, v166
	v_add_u32_e32 v172, 0xe2, v166
	v_add_u32_e32 v173, 0xc3, v166
	v_add_u32_e32 v174, 0xe3, v166
	v_add_u32_e32 v175, 0xc8, v166
	v_add_u32_e32 v176, 0xe8, v166
	v_add_u32_e32 v177, 0xc9, v166
	v_add_u32_e32 v178, 0xe9, v166
	v_add_u32_e32 v179, 0xca, v166
	v_add_u32_e32 v180, 0xea, v166
	v_add_u32_e32 v181, 0xcb, v166
	v_add_u32_e32 v182, 0xeb, v166
	v_add_u32_e32 v183, 0xd0, v166
	v_add_u32_e32 v184, 0xf0, v166
	v_add_u32_e32 v185, 0xd1, v166
	v_add_u32_e32 v186, 0xf1, v166
	v_add_u32_e32 v187, 0xd2, v166
	v_add_u32_e32 v188, 0xf2, v166
	v_add_u32_e32 v189, 0xd3, v166
	v_add_u32_e32 v190, 0xf3, v166
	v_add_u32_e32 v191, 0xd8, v166
	v_add_u32_e32 v192, 0xf8, v166
	v_add_u32_e32 v193, 0xd9, v166
	v_add_u32_e32 v194, 0xf9, v166
	v_add_u32_e32 v195, 0xda, v166
	v_add_u32_e32 v196, 0xfa, v166
	v_add_u32_e32 v197, 0xdb, v166
	v_add_u32_e32 v166, 0xfb, v166
	v_cmp_lt_i32_e64 s[44:45], v167, v163
	v_cmp_lt_i32_e64 s[6:7], v168, v163
	v_cmp_lt_i32_e64 s[68:69], v169, v163
	v_cmp_lt_i32_e64 s[0:1], v170, v163
	v_cmp_lt_i32_e64 s[72:73], v171, v163
	v_cmp_lt_i32_e64 s[40:41], v172, v163
	v_cmp_lt_i32_e64 s[76:77], v173, v163
	v_cmp_lt_i32_e64 s[42:43], v174, v163
	v_cmp_lt_i32_e64 s[78:79], v175, v163
	v_cmp_lt_i32_e64 s[48:49], v176, v163
	v_cmp_lt_i32_e64 s[80:81], v177, v163
	v_cmp_lt_i32_e64 s[50:51], v178, v163
	v_cmp_lt_i32_e64 s[82:83], v179, v163
	v_cmp_lt_i32_e64 s[52:53], v180, v163
	v_cmp_lt_i32_e64 s[84:85], v181, v163
	v_cmp_lt_i32_e64 s[54:55], v182, v163
	v_cmp_lt_i32_e64 s[88:89], v183, v163
	v_cmp_lt_i32_e64 s[58:59], v184, v163
	v_cmp_lt_i32_e64 s[90:91], v185, v163
	v_cmp_lt_i32_e64 s[60:61], v186, v163
	v_cmp_lt_i32_e64 s[92:93], v187, v163
	v_cmp_lt_i32_e64 s[62:63], v188, v163
	v_cmp_lt_i32_e64 s[94:95], v189, v163
	v_cmp_lt_i32_e64 s[64:65], v190, v163
	v_cmp_lt_i32_e64 s[96:97], v191, v163
	v_cmp_lt_i32_e64 s[66:67], v192, v163
	v_cmp_lt_i32_e64 s[4:5], v193, v163
	v_cmp_lt_i32_e64 s[70:71], v194, v163
	v_cmp_lt_i32_e32 vcc, v195, v163
	v_cmp_lt_i32_e64 s[74:75], v196, v163
	v_cmp_lt_i32_e64 s[86:87], v197, v163
	v_cmp_lt_i32_e64 s[56:57], v166, v163
	s_nop 1
	s_or_b64 vcc, s[86:87], vcc
	v_cndmask_b32_e32 v78, 0, v78, vcc
	s_or_b64 vcc, vcc, s[4:5]
	v_cndmask_b32_e32 v75, 0, v75, vcc
	s_or_b64 vcc, vcc, s[96:97]
	v_cndmask_b32_e32 v74, 0, v74, vcc
	s_or_b64 vcc, vcc, s[94:95]
	v_cndmask_b32_e32 v71, 0, v71, vcc
	s_or_b64 vcc, vcc, s[92:93]
	v_cndmask_b32_e32 v70, 0, v70, vcc
	s_or_b64 vcc, vcc, s[90:91]
	v_cndmask_b32_e32 v67, 0, v67, vcc
	s_or_b64 vcc, vcc, s[88:89]
	v_cndmask_b32_e32 v66, 0, v66, vcc
	s_or_b64 vcc, vcc, s[84:85]
	v_cndmask_b32_e32 v63, 0, v63, vcc
	s_or_b64 vcc, vcc, s[82:83]
	v_cndmask_b32_e32 v62, 0, v62, vcc
	s_or_b64 vcc, vcc, s[80:81]
	v_cndmask_b32_e32 v59, 0, v59, vcc
	s_or_b64 vcc, vcc, s[78:79]
	v_cndmask_b32_e32 v58, 0, v58, vcc
	s_or_b64 vcc, vcc, s[76:77]
	v_cndmask_b32_e32 v55, 0, v55, vcc
	s_or_b64 vcc, vcc, s[72:73]
	v_cndmask_b32_e32 v54, 0, v54, vcc
	s_or_b64 vcc, vcc, s[68:69]
	v_cndmask_b32_e32 v1, 0, v1, vcc
	s_or_b64 vcc, vcc, s[44:45]
	v_cndmask_b32_e32 v2, 0, v2, vcc
	s_or_b64 vcc, s[56:57], s[74:75]
	v_cndmask_b32_e32 v80, 0, v80, vcc
	s_or_b64 vcc, vcc, s[70:71]
	v_cndmask_b32_e32 v77, 0, v77, vcc
	s_or_b64 vcc, vcc, s[66:67]
	v_cndmask_b32_e32 v76, 0, v76, vcc
	s_or_b64 vcc, vcc, s[64:65]
	v_cndmask_b32_e32 v73, 0, v73, vcc
	s_or_b64 vcc, vcc, s[62:63]
	v_cndmask_b32_e32 v72, 0, v72, vcc
	s_or_b64 vcc, vcc, s[60:61]
	v_cndmask_b32_e32 v69, 0, v69, vcc
	s_or_b64 vcc, vcc, s[58:59]
	v_cndmask_b32_e32 v68, 0, v68, vcc
	s_or_b64 vcc, vcc, s[54:55]
	v_cndmask_b32_e32 v65, 0, v65, vcc
	s_or_b64 vcc, vcc, s[52:53]
	v_cndmask_b32_e32 v64, 0, v64, vcc
	s_or_b64 vcc, vcc, s[50:51]
	v_cndmask_b32_e32 v61, 0, v61, vcc
	s_or_b64 vcc, vcc, s[48:49]
	v_cndmask_b32_e32 v60, 0, v60, vcc
	s_or_b64 vcc, vcc, s[42:43]
	v_cndmask_b32_e32 v57, 0, v57, vcc
	s_or_b64 vcc, vcc, s[40:41]
	v_cndmask_b32_e32 v56, 0, v56, vcc
	s_or_b64 vcc, vcc, s[0:1]
	v_cndmask_b32_e32 v53, 0, v53, vcc
	s_or_b64 vcc, vcc, s[6:7]
	v_cndmask_b32_e64 v79, 0, v79, s[86:87]
	v_cndmask_b32_e32 v52, 0, v52, vcc
	v_cndmask_b32_e64 v81, 0, v81, s[56:57]
; __device__ __forceinline__ unsigned cvt_pk_bf16(float lo, float hi) { unsigned r; asm volatile("v_cvt_pk_bf16_f32 %0, %1, %2" : "=v"(r) : "v"(lo), "v"(hi)); return r; }
; __device__ __forceinline__ float ex2(float x) { return __builtin_amdgcn_exp2f(x); }
; __device__ __forceinline__ f32x16 mfma32(bf16x8 a, bf16x8 b, f32x16 c) { return __builtin_amdgcn_mfma_f32_32x32x16_bf16(a, b, c, 0, 0, 0); }
; __device__ __forceinline__ void sb_unit(int b, int h, int qb, const bf16_t* __restrict__ PROJ, bf16_t* OCAT, float* SSQO, ldsp shm, volatile LAS unsigned* FL) {
;     ...
;             for (int r = 0; r < 16; ++r) { tot += l0[r] + l1[r]; z0[r] += l0[r]; z1[r] += l1[r]; }
;             u32x4 lh[4];
; #pragma unroll
;             for (int k = 0; k < 4; ++k)
; #pragma unroll
;                 for (int j = 0; j < 4; ++j) { const float a = (k < 2) ? l0[(k & 1) * 8 + 2 * j] : l1[(k & 1) * 8 + 2 * j], c = (k < 2) ? l0[(k & 1) * 8 + 2 * j + 1] : l1[(k & 1) * 8 + 2 * j + 1];
;                     lh[k][j] = cvt_pk_bf16(a, c); }
;     ...
;             f32x16 x0, x1;
; #pragma unroll
;             for (int r = 0; r < 16; ++r) { x0[r] = Lc; x1[r] = Lc; }
;             x0 = mfma32(Ta, SB_B(lh[0]), x0); x0 = mfma32(Tb, SB_B(lh[1]), x0); x0 = mfma32(Ton, SB_B(lh[2]), x0); x0 = mfma32(Ton, SB_B(lh[3]), x0);
;             x1 = mfma32(Ta, SB_B(lh[2]), x1); x1 = mfma32(Tb, SB_B(lh[3]), x1);
;     ...
; #pragma unroll
;             for (int r = 0; r < 16; ++r) { z0[r] = ex2(z0[r] + x0[r]); z1[r] = ex2(z1[r] + x1[r]); }
.LBB0_1058:
	v_mov_b32_e32 v37, v36
	v_mov_b32_e32 v38, v36
	v_mov_b32_e32 v39, v36
	v_mov_b32_e32 v40, v36
	v_mov_b32_e32 v41, v36
	v_mov_b32_e32 v42, v36
	v_mov_b32_e32 v43, v36
	v_mov_b32_e32 v44, v36
	v_mov_b32_e32 v45, v36
	v_mov_b32_e32 v46, v36
	v_mov_b32_e32 v47, v36
	v_mov_b32_e32 v48, v36
	v_mov_b32_e32 v49, v36
	v_mov_b32_e32 v50, v36
	v_mov_b32_e32 v51, v36
	v_cvt_pk_bf16_f32 v200, v2, v1
	v_cvt_pk_bf16_f32 v201, v54, v55
	v_cvt_pk_bf16_f32 v202, v58, v59
	v_cvt_pk_bf16_f32 v203, v62, v63
	v_readlane_b32 s4, v254, 39
	s_nop 0
	v_mfma_f32_32x32x16_bf16 v[114:129], v[150:153], v[200:203], v[36:51]
	v_cvt_pk_bf16_f32 v200, v66, v67
	v_cvt_pk_bf16_f32 v201, v70, v71
	v_cvt_pk_bf16_f32 v202, v74, v75
	v_cvt_pk_bf16_f32 v203, v78, v79
	v_readlane_b32 s6, v254, 41
	v_readlane_b32 s7, v254, 42
	v_readlane_b32 s5, v254, 40
	v_mfma_f32_32x32x16_bf16 v[114:129], v[146:149], v[200:203], v[114:129]
	s_mov_b32 s6, s4
	s_mov_b32 s7, s4
	s_mov_b32 s5, s4
	v_mov_b64_e32 v[206:207], s[6:7]
	v_mov_b64_e32 v[204:205], s[4:5]
	v_cvt_pk_bf16_f32 v200, v52, v53
	v_cvt_pk_bf16_f32 v201, v56, v57
	v_cvt_pk_bf16_f32 v202, v60, v61
	v_cvt_pk_bf16_f32 v203, v64, v65
	v_cvt_pk_bf16_f32 v208, v68, v69
	v_cvt_pk_bf16_f32 v209, v72, v73
	v_cvt_pk_bf16_f32 v210, v76, v77
	v_cvt_pk_bf16_f32 v211, v80, v81
	v_sub_f32_e32 v98, v98, v2
	s_nop 0
	v_mfma_f32_32x32x16_bf16 v[114:129], v[204:207], v[200:203], v[114:129]
	v_sub_f32_e32 v99, v99, v1
	v_sub_f32_e32 v100, v100, v54
	v_sub_f32_e32 v101, v101, v55
	v_sub_f32_e32 v102, v102, v58
	v_sub_f32_e32 v103, v103, v59
	v_sub_f32_e32 v104, v104, v62
	v_sub_f32_e32 v105, v105, v63
	v_mfma_f32_32x32x16_bf16 v[114:129], v[204:207], v[208:211], v[114:129]
	v_sub_f32_e32 v106, v106, v66
	v_sub_f32_e32 v107, v107, v67
	v_sub_f32_e32 v108, v108, v70
	v_sub_f32_e32 v109, v109, v71
	v_sub_f32_e32 v110, v110, v74
	v_sub_f32_e32 v111, v111, v75
	v_sub_f32_e32 v112, v112, v78
	v_sub_f32_e32 v113, v113, v79
	s_nop 3
	v_sub_f32_e32 v114, v98, v114
	v_sub_f32_e32 v115, v99, v115
	v_sub_f32_e32 v116, v100, v116
	v_sub_f32_e32 v117, v101, v117
	v_sub_f32_e32 v118, v102, v118
	v_sub_f32_e32 v119, v103, v119
	v_sub_f32_e32 v120, v104, v120
	v_sub_f32_e32 v121, v105, v121
	v_sub_f32_e32 v122, v106, v122
	v_sub_f32_e32 v123, v107, v123
	v_sub_f32_e32 v124, v108, v124
	v_sub_f32_e32 v125, v109, v125
	v_sub_f32_e32 v126, v110, v126
	v_sub_f32_e32 v127, v111, v127
	v_sub_f32_e32 v128, v112, v128
	v_sub_f32_e32 v129, v113, v129
	v_mov_b64_e32 v[112:113], v[50:51]
	v_mov_b64_e32 v[110:111], v[48:49]
	v_mov_b64_e32 v[108:109], v[46:47]
	v_mov_b64_e32 v[106:107], v[44:45]
	v_mov_b64_e32 v[104:105], v[42:43]
	v_mov_b64_e32 v[102:103], v[40:41]
	v_mov_b64_e32 v[100:101], v[38:39]
	v_mov_b64_e32 v[98:99], v[36:37]
	v_sub_f32_e32 v37, v82, v52
	v_sub_f32_e32 v38, v83, v53
	v_mfma_f32_32x32x16_bf16 v[98:113], v[150:153], v[200:203], v[98:113]
	v_sub_f32_e32 v39, v84, v56
	v_sub_f32_e32 v40, v85, v57
	v_sub_f32_e32 v41, v86, v60
	v_sub_f32_e32 v42, v87, v61
	v_sub_f32_e32 v43, v88, v64
	v_sub_f32_e32 v44, v89, v65
	v_sub_f32_e32 v45, v90, v68
	v_mfma_f32_32x32x16_bf16 v[98:113], v[146:149], v[208:211], v[98:113]
	v_sub_f32_e32 v46, v91, v69
	v_sub_f32_e32 v47, v92, v72
	v_sub_f32_e32 v48, v93, v73
	v_sub_f32_e32 v49, v94, v76
	v_sub_f32_e32 v50, v95, v77
	v_sub_f32_e32 v51, v96, v80
	v_sub_f32_e32 v82, v97, v81
	s_mov_b32 s0, s4
	s_nop 3
	v_sub_f32_e32 v37, v37, v98
	v_sub_f32_e32 v85, v38, v99
	v_sub_f32_e32 v39, v39, v100
	v_sub_f32_e32 v40, v40, v101
	v_sub_f32_e32 v86, v41, v102
	v_sub_f32_e32 v89, v42, v103
	v_sub_f32_e32 v43, v43, v104
	v_sub_f32_e32 v44, v44, v105
	v_sub_f32_e32 v90, v45, v106
	v_sub_f32_e32 v93, v46, v107
	v_sub_f32_e32 v47, v47, v108
	v_sub_f32_e32 v48, v48, v109
	v_sub_f32_e32 v97, v49, v110
	v_sub_f32_e32 v98, v50, v111
	v_sub_f32_e32 v51, v51, v112
	v_sub_f32_e32 v99, v82, v113
	v_writelane_b32 v254, s0, 39
	v_exp_f32_e32 v84, v114
	v_exp_f32_e32 v38, v37
	v_exp_f32_e32 v83, v115
	v_exp_f32_e32 v37, v85
	v_exp_f32_e32 v88, v116
	v_exp_f32_e32 v42, v39
	v_exp_f32_e32 v87, v117
	v_exp_f32_e32 v41, v40
	v_exp_f32_e32 v92, v118
	v_exp_f32_e32 v46, v86
	v_exp_f32_e32 v91, v119
	v_exp_f32_e32 v45, v89
	v_exp_f32_e32 v96, v120
	v_exp_f32_e32 v50, v43
	v_exp_f32_e32 v95, v121
	v_exp_f32_e32 v49, v44
	v_exp_f32_e32 v86, v122
	v_exp_f32_e32 v40, v90
	v_exp_f32_e32 v85, v123
	v_exp_f32_e32 v39, v93
	v_exp_f32_e32 v90, v124
	v_exp_f32_e32 v44, v47
	v_exp_f32_e32 v89, v125
	v_exp_f32_e32 v43, v48
	v_exp_f32_e32 v94, v126
	v_exp_f32_e32 v48, v97
	v_exp_f32_e32 v93, v127
	v_exp_f32_e32 v47, v98
	v_exp_f32_e32 v98, v128
	v_exp_f32_e32 v82, v51
	v_exp_f32_e32 v97, v129
	v_exp_f32_e32 v51, v99
	v_writelane_b32 v254, s1, 40
	v_writelane_b32 v254, s2, 41
	v_writelane_b32 v254, s3, 42
	s_andn2_b64 vcc, exec, s[16:17]
	s_cbranch_vccnz .LBB0_1060
; #define LAS __attribute__((address_space(3)))
; __device__ __forceinline__ float swapsum(float m) { auto rr = __builtin_amdgcn_permlane32_swap(__float_as_uint(m), __float_as_uint(m), false, false); return __uint_as_float(rr[0]) + __uint_as_float(rr[1]); }
; __device__ __forceinline__ u32x4 packp(const f32x16& p, int b) { u32x4 w; w.x = cvt_pk_bf16(p[b], p[b + 1]); w.y = cvt_pk_bf16(p[b + 2], p[b + 3]); w.z = cvt_pk_bf16(p[b + 4], p[b + 5]); w.w = cvt_pk_bf16(p[b + 6], p[b + 7]); return w; }
; __device__ __forceinline__ void sb_unit(int b, int h, int qb, const bf16_t* __restrict__ PROJ, bf16_t* OCAT, float* SSQO, ldsp shm, volatile LAS unsigned* FL) {
;     ...
;             if (diag) {
; #pragma unroll
;                 for (int r = 0; r < 16; ++r) { const int kk = kb0 + (r & 3) + 8 * (r >> 2); if (kk >= qabs) z0[r] = 0.f; if (kk + 32 >= qabs) z1[r] = 0.f; } }
;             pv(o, vp0 + (step & 3) * VS, packp(z0, 0), packp(z0, 8), packp(z1, 0), packp(z1, 8));
;             Lc += swapsum(tot);
;             wfin = __all(Lc <= SB_DONE) != 0;
;         }
;         if (t == 0) wfin = true;
;         if (wfin && lane == 0) __hip_atomic_fetch_or((LAS unsigned*)&FL[step % 3], 1u << wid, __ATOMIC_RELAXED, __HIP_MEMORY_SCOPE_WORKGROUP);
	v_cmp_lt_i32_e64 s[92:93], v195, v163
	v_cmp_lt_i32_e64 s[94:95], v197, v163
	v_cmp_lt_i32_e64 s[90:91], v193, v163
	s_or_b64 s[92:93], s[94:95], s[92:93]
	v_cmp_lt_i32_e64 s[88:89], v191, v163
	s_or_b64 s[90:91], s[92:93], s[90:91]
	v_cmp_lt_i32_e64 s[86:87], v189, v163
	s_or_b64 s[88:89], s[90:91], s[88:89]
	v_cmp_lt_i32_e64 s[84:85], v187, v163
	s_or_b64 s[86:87], s[88:89], s[86:87]
	v_cmp_lt_i32_e64 s[82:83], v185, v163
	s_or_b64 s[84:85], s[86:87], s[84:85]
	v_cmp_lt_i32_e64 s[80:81], v183, v163
	s_or_b64 s[82:83], s[84:85], s[82:83]
	v_cmp_lt_i32_e64 s[78:79], v181, v163
	s_or_b64 s[80:81], s[82:83], s[80:81]
	v_cmp_lt_i32_e64 s[76:77], v179, v163
	s_or_b64 s[78:79], s[80:81], s[78:79]
	v_cmp_lt_i32_e64 s[74:75], v177, v163
	s_or_b64 s[76:77], s[78:79], s[76:77]
	v_cmp_lt_i32_e64 s[72:73], v175, v163
	s_or_b64 s[74:75], s[76:77], s[74:75]
	v_cmp_lt_i32_e64 s[70:71], v173, v163
	s_or_b64 s[72:73], s[74:75], s[72:73]
	v_cmp_lt_i32_e64 s[6:7], v171, v163
	s_or_b64 s[70:71], s[72:73], s[70:71]
	v_cmp_lt_i32_e64 s[4:5], v169, v163
	s_or_b64 s[6:7], s[70:71], s[6:7]
	v_cmp_lt_i32_e32 vcc, v167, v163
	s_or_b64 s[4:5], s[6:7], s[4:5]
	s_or_b64 vcc, s[4:5], vcc
	v_cmp_lt_i32_e64 s[68:69], v196, v163
	v_cndmask_b32_e32 v84, 0, v84, vcc
	v_cmp_lt_i32_e32 vcc, v166, v163
	v_cmp_lt_i32_e64 s[66:67], v194, v163
	v_cndmask_b32_e64 v83, 0, v83, s[4:5]
	s_or_b64 s[4:5], vcc, s[68:69]
	v_cmp_lt_i32_e64 s[64:65], v192, v163
	v_cndmask_b32_e64 v82, 0, v82, s[4:5]
	s_or_b64 s[4:5], s[4:5], s[66:67]
	v_cmp_lt_i32_e64 s[62:63], v190, v163
	v_cndmask_b32_e64 v47, 0, v47, s[4:5]
	s_or_b64 s[4:5], s[4:5], s[64:65]
	v_cmp_lt_i32_e64 s[60:61], v188, v163
	v_cndmask_b32_e64 v48, 0, v48, s[4:5]
	s_or_b64 s[4:5], s[4:5], s[62:63]
	v_cmp_lt_i32_e64 s[58:59], v186, v163
	v_cndmask_b32_e64 v43, 0, v43, s[4:5]
	s_or_b64 s[4:5], s[4:5], s[60:61]
	v_cmp_lt_i32_e64 s[56:57], v184, v163
	v_cndmask_b32_e64 v44, 0, v44, s[4:5]
	s_or_b64 s[4:5], s[4:5], s[58:59]
	v_cmp_lt_i32_e64 s[54:55], v182, v163
	v_cndmask_b32_e64 v39, 0, v39, s[4:5]
	s_or_b64 s[4:5], s[4:5], s[56:57]
	v_cmp_lt_i32_e64 s[52:53], v180, v163
	v_cndmask_b32_e64 v40, 0, v40, s[4:5]
	s_or_b64 s[4:5], s[4:5], s[54:55]
	v_cmp_lt_i32_e64 s[50:51], v178, v163
	v_cndmask_b32_e64 v49, 0, v49, s[4:5]
	s_or_b64 s[4:5], s[4:5], s[52:53]
	v_cmp_lt_i32_e64 s[48:49], v176, v163
	v_cndmask_b32_e64 v50, 0, v50, s[4:5]
	s_or_b64 s[4:5], s[4:5], s[50:51]
	v_cmp_lt_i32_e64 s[44:45], v174, v163
	v_cndmask_b32_e64 v45, 0, v45, s[4:5]
	s_or_b64 s[4:5], s[4:5], s[48:49]
	v_cmp_lt_i32_e64 s[42:43], v172, v163
	v_cndmask_b32_e64 v46, 0, v46, s[4:5]
	s_or_b64 s[4:5], s[4:5], s[44:45]
	v_cmp_lt_i32_e64 s[40:41], v170, v163
	v_cndmask_b32_e64 v41, 0, v41, s[4:5]
	s_or_b64 s[4:5], s[4:5], s[42:43]
	v_cmp_lt_i32_e64 s[0:1], v168, v163
	v_cndmask_b32_e64 v42, 0, v42, s[4:5]
	s_or_b64 s[4:5], s[4:5], s[40:41]
	s_or_b64 s[0:1], s[4:5], s[0:1]
	v_cndmask_b32_e64 v98, 0, v98, s[92:93]
	v_cndmask_b32_e64 v93, 0, v93, s[90:91]
	v_cndmask_b32_e64 v94, 0, v94, s[88:89]
	v_cndmask_b32_e64 v89, 0, v89, s[86:87]
	v_cndmask_b32_e64 v90, 0, v90, s[84:85]
	v_cndmask_b32_e64 v85, 0, v85, s[82:83]
	v_cndmask_b32_e64 v86, 0, v86, s[80:81]
	v_cndmask_b32_e64 v95, 0, v95, s[78:79]
	v_cndmask_b32_e64 v96, 0, v96, s[76:77]
	v_cndmask_b32_e64 v91, 0, v91, s[74:75]
	v_cndmask_b32_e64 v92, 0, v92, s[72:73]
	v_cndmask_b32_e64 v87, 0, v87, s[70:71]
	v_cndmask_b32_e64 v88, 0, v88, s[6:7]
	v_cndmask_b32_e64 v97, 0, v97, s[94:95]
	v_cndmask_b32_e64 v37, 0, v37, s[4:5]
	v_cndmask_b32_e64 v38, 0, v38, s[0:1]
	v_cndmask_b32_e32 v51, 0, v51, vcc
.LBB0_1060:
	v_add_f32_e32 v2, v2, v52
	v_add_f32_e32 v1, v1, v53
	v_add_f32_e32 v2, 0, v2
	v_add_f32_e32 v52, v54, v56
	v_add_f32_e32 v1, v1, v2
	v_add_f32_e32 v53, v55, v57
	v_add_f32_e32 v1, v52, v1
	v_add_f32_e32 v54, v58, v60
	v_add_f32_e32 v1, v53, v1
	v_add_f32_e32 v55, v59, v61
	v_add_f32_e32 v1, v54, v1
	v_add_f32_e32 v56, v62, v64
	v_add_f32_e32 v1, v55, v1
	v_add_f32_e32 v57, v63, v65
	v_add_f32_e32 v1, v56, v1
	v_add_f32_e32 v58, v66, v68
	v_add_f32_e32 v1, v57, v1
	v_add_f32_e32 v59, v67, v69
	v_add_f32_e32 v1, v58, v1
	v_add_f32_e32 v60, v70, v72
	v_add_f32_e32 v1, v59, v1
	v_add_f32_e32 v61, v71, v73
	v_add_f32_e32 v1, v60, v1
	v_add_f32_e32 v62, v74, v76
	v_add_f32_e32 v1, v61, v1
	v_add_f32_e32 v63, v75, v77
	v_add_f32_e32 v1, v62, v1
	v_add_f32_e32 v64, v78, v80
	v_add_f32_e32 v1, v63, v1
	v_add_f32_e32 v65, v79, v81
	v_add_f32_e32 v1, v64, v1
	v_add_u32_e32 v2, s8, v162
	v_add_f32_e32 v1, v65, v1
	v_cvt_pk_bf16_f32 v56, v84, v83
	v_cvt_pk_bf16_f32 v57, v88, v87
	v_cvt_pk_bf16_f32 v58, v92, v91
	v_cvt_pk_bf16_f32 v59, v96, v95
	v_cvt_pk_bf16_f32 v60, v86, v85
	v_cvt_pk_bf16_f32 v61, v90, v89
	v_cvt_pk_bf16_f32 v62, v94, v93
	v_cvt_pk_bf16_f32 v63, v98, v97
	v_cvt_pk_bf16_f32 v52, v38, v37
	v_cvt_pk_bf16_f32 v53, v42, v41
	v_cvt_pk_bf16_f32 v54, v46, v45
	v_cvt_pk_bf16_f32 v55, v50, v49
	v_cvt_pk_bf16_f32 v38, v40, v39
	v_cvt_pk_bf16_f32 v39, v44, v43
	v_cvt_pk_bf16_f32 v40, v48, v47
	v_cvt_pk_bf16_f32 v41, v82, v51
	ds_read_b64_tr_b16 v[42:43], v2 offset:32768
	ds_read_b64_tr_b16 v[44:45], v2 offset:33280
	ds_read_b64_tr_b16 v[46:47], v2 offset:33792
	ds_read_b64_tr_b16 v[48:49], v2 offset:34304
	ds_read_b64_tr_b16 v[64:65], v2 offset:34816
	ds_read_b64_tr_b16 v[66:67], v2 offset:35328
	ds_read_b64_tr_b16 v[68:69], v2 offset:35840
	ds_read_b64_tr_b16 v[70:71], v2 offset:36352
	s_waitcnt lgkmcnt(0)
	v_mfma_f32_32x32x16_bf16 v[20:35], v[56:59], v[42:45], v[20:35]
	s_mov_b32 s0, 0x43160000
	s_movk_i32 s80, 0xff
	s_mov_b32 s81, 0x41000000
	s_mov_b64 s[82:83], 0x800
	s_mov_b64 s[84:85], 0xc00
	s_mov_b64 s[86:87], 0x70000
	s_mov_b64 s[88:89], 0x70080
	v_mfma_f32_32x32x16_bf16 v[20:35], v[60:63], v[46:49], v[20:35]
	v_mfma_f32_32x32x16_bf16 v[20:35], v[52:55], v[64:67], v[20:35]
	v_mfma_f32_32x32x16_bf16 v[20:35], v[38:41], v[68:71], v[20:35]
	ds_read_b64_tr_b16 v[42:43], v2 offset:36864
	ds_read_b64_tr_b16 v[44:45], v2 offset:37376
	ds_read_b64_tr_b16 v[46:47], v2 offset:37888
	ds_read_b64_tr_b16 v[48:49], v2 offset:38400
	ds_read_b64_tr_b16 v[64:65], v2 offset:38912
	ds_read_b64_tr_b16 v[66:67], v2 offset:39424
	ds_read_b64_tr_b16 v[68:69], v2 offset:39936
	ds_read_b64_tr_b16 v[70:71], v2 offset:40448
	v_mov_b32_e32 v2, v1
	s_nop 1
	v_permlane32_swap_b32_e32 v1, v2
	v_add_f32_e32 v1, v1, v2
	v_add_f32_e32 v36, v36, v1
	v_cmp_le_f32_e32 vcc, s0, v36
	s_waitcnt lgkmcnt(0)
	v_mfma_f32_32x32x16_bf16 v[4:19], v[56:59], v[42:45], v[4:19]
	s_cmp_eq_u64 vcc, exec
	s_cselect_b64 s[0:1], -1, 0
	v_mfma_f32_32x32x16_bf16 v[4:19], v[60:63], v[46:49], v[4:19]
	v_mfma_f32_32x32x16_bf16 v[4:19], v[52:55], v[64:67], v[4:19]
	v_mfma_f32_32x32x16_bf16 v[4:19], v[38:41], v[68:71], v[4:19]
